# stacked deletions on v_kpf: P2 loop-edge edits + shift/mask unit-scheduler division (P1/P7/P8) + 32 dead v_readlane restores removed from the GEMM unit loops
# baseline (speedup 1.0000x reference)
.LBB0_159:
	v_readlane_b32 s56, v239, 42
	v_readlane_b32 s57, v239, 43
	v_readlane_b32 s58, v239, 44
	v_readlane_b32 s59, v239, 45
	s_mov_b64 s[62:63], s[56:57]
	s_cbranch_execnz .LBB0_147
	s_branch .LBB0_148

.LBB0_994:
	s_ashr_i32 s36, s34, 3
	s_lshl_b32 s2, s34, 7
	s_ashr_i32 s37, s36, 31
	s_and_b32 s2, s2, 0x380
	s_lshl_b64 s[36:37], s[36:37], 13
	v_readlane_b32 s86, v239, 13
	v_or_b32_e32 v2, s2, v219
	v_readlane_b32 s87, v239, 14
	s_add_u32 s36, s86, s36
	s_waitcnt vmcnt(0)
	s_addc_u32 s37, s87, s37
	v_lshlrev_b32_e32 v4, 2, v2
	v_mov_b32_e32 v5, v199
	global_load_dwordx4 v[26:29], v4, s[36:37]
	global_load_dwordx4 v[30:33], v4, s[36:37] offset:16
	v_lshl_add_u64 v[4:5], s[36:37], 0, v[4:5]
	s_mov_b64 s[36:37], 0x1000
	s_movk_i32 s2, 0x1000
	v_lshl_add_u64 v[6:7], v[4:5], 0, s[36:37]
	v_add_co_u32_e32 v4, vcc, s2, v4
	v_mov_b32_e32 v8, v186
	s_nop 0
	v_addc_co_u32_e32 v5, vcc, 0, v5, vcc
	global_load_dwordx4 v[34:37], v[4:5], off
	global_load_dwordx4 v[38:41], v[6:7], off offset:16
	v_mov_b32_e32 v6, v190
	v_mov_b32_e32 v14, v178
	v_mov_b32_e32 v24, v183
	v_mov_b32_e32 v20, v192
	v_lshl_add_u32 v4, s96, 8, v218
	v_ashrrev_i32_e32 v5, 31, v4
	v_lshlrev_b64 v[4:5], 10, v[4:5]
	v_mov_b32_e32 v3, v199
	v_mov_b32_e32 v12, v182
	v_mov_b32_e32 v42, v179
	v_mov_b32_e32 v22, v188
	v_lshl_add_u64 v[4:5], s[58:59], 0, v[4:5]
	v_lshl_add_u64 v[2:3], v[4:5], 0, v[2:3]
	v_lshl_add_u64 v[2:3], v[2:3], 0, v[204:205]
	s_mov_b32 s2, 0x8000
	s_waitcnt vmcnt(0)
	v_mov_b32_e32 v7, v26
	v_mov_b32_e32 v9, v30
	v_pk_mul_f32 v[16:17], v[8:9], s[24:25]
	v_mov_b32_e32 v26, v191
	v_sub_f32_e32 v16, v16, v17
	v_mov_b32_e32 v21, v28
	v_pk_mul_f32 v[10:11], v[26:27], s[24:25]
	v_max_f32_e32 v16, 0xc1898193, v16
	v_pk_mul_f32 v[18:19], v[6:7], s[24:25]
	v_pk_mul_f32 v[6:7], v[20:21], s[24:25]
	v_add_f32_e32 v25, 1.0, v35
	v_add_f32_e32 v15, 1.0, v38
	v_sub_f32_e32 v10, v10, v11
	v_pk_mul_f32 v[20:21], v[14:15], s[26:27]
	v_pk_mul_f32 v[14:15], v[24:25], s[26:27]
	v_exp_f32_e32 v25, v16
	v_max_f32_e32 v10, 0xc1898193, v10
	v_sub_f32_e32 v18, v18, v19
	v_sub_f32_e32 v6, v6, v7
	v_exp_f32_e32 v26, v10
	v_sub_f32_e32 v14, v14, v15
	v_max_f32_e32 v18, 0xc1898193, v18
	v_max_f32_e32 v6, 0xc1898193, v6
	v_med3_f32 v14, v14, s71, v223
	v_mov_b32_e32 v30, v187
	v_mov_b32_e32 v23, v32
	v_add_f32_e32 v13, 1.0, v34
	v_add_f32_e32 v43, 1.0, v39
	v_exp_f32_e32 v24, v18
	v_sub_f32_e32 v20, v20, v21
	v_exp_f32_e32 v28, v6
	v_mul_f32_e32 v10, v10, v14
	v_add_f32_e32 v14, 1.0, v25
	v_pk_mul_f32 v[8:9], v[30:31], s[24:25]
	v_pk_mul_f32 v[4:5], v[22:23], s[24:25]
	v_pk_mul_f32 v[22:23], v[12:13], s[26:27]
	v_pk_mul_f32 v[12:13], v[42:43], s[26:27]
	v_med3_f32 v20, v20, s71, v223
	v_rcp_f32_e32 v14, v14
	v_sub_f32_e32 v8, v8, v9
	v_sub_f32_e32 v12, v12, v13
	v_mul_f32_e32 v16, v16, v20
	v_add_f32_e32 v20, 1.0, v26
	v_max_f32_e32 v8, 0xc1898193, v8
	v_med3_f32 v12, v12, s71, v223
	v_rcp_f32_e32 v20, v20
	v_exp_f32_e32 v27, v8
	v_mul_f32_e32 v8, v8, v12
	v_add_f32_e32 v12, 1.0, v24
	v_add_f32_e32 v24, 1.0, v28
	v_mul_f32_e32 v14, v14, v16
	v_rcp_f32_e32 v16, v24
	v_add_f32_e32 v25, 1.0, v36
	v_mov_b32_e32 v24, v184
	v_sub_f32_e32 v22, v22, v23
	v_pk_mul_f32 v[24:25], v[24:25], s[26:27]
	v_sub_f32_e32 v4, v4, v5
	v_med3_f32 v22, v22, s71, v223
	v_mul_f32_e32 v10, v20, v10
	v_sub_f32_e32 v20, v24, v25
	v_max_f32_e32 v4, 0xc1898193, v4
	v_mul_f32_e32 v18, v18, v22
	v_add_f32_e32 v22, 1.0, v27
	v_med3_f32 v20, v20, s71, v223
	v_add_f32_e32 v27, 1.0, v40
	v_mov_b32_e32 v26, v180
	v_exp_f32_e32 v30, v4
	v_rcp_f32_e32 v12, v12
	v_mul_f32_e32 v6, v6, v20
	v_pk_mul_f32 v[26:27], v[26:27], s[26:27]
	v_rcp_f32_e32 v22, v22
	v_mul_f32_e32 v6, v16, v6
	v_sub_f32_e32 v16, v26, v27
	v_mov_b32_e32 v28, v193
	v_med3_f32 v16, v16, s71, v223
	v_pk_mul_f32 v[28:29], v[28:29], s[24:25]
	v_mul_f32_e32 v4, v4, v16
	v_sub_f32_e32 v16, v28, v29
	v_mov_b32_e32 v32, v189
	v_mul_f32_e32 v12, v12, v18
	v_add_f32_e32 v18, 1.0, v30
	v_max_f32_e32 v16, 0xc1898193, v16
	v_pk_mul_f32 v[30:31], v[32:33], s[24:25]
	v_mul_f32_e32 v8, v22, v8
	v_rcp_f32_e32 v18, v18
	v_sub_f32_e32 v20, v30, v31
	v_exp_f32_e32 v22, v16
	v_max_f32_e32 v20, 0xc1898193, v20
	v_exp_f32_e32 v24, v20
	v_mul_f32_e32 v4, v18, v4
	v_add_f32_e32 v18, 1.0, v22
	v_add_f32_e32 v33, 1.0, v37
	v_mov_b32_e32 v32, v185
	v_rcp_f32_e32 v18, v18
	v_pk_mul_f32 v[32:33], v[32:33], s[26:27]
	v_mov_b32_e32 v36, v199
	v_add_f32_e32 v22, 1.0, v24
	v_sub_f32_e32 v24, v32, v33
	v_cvt_pk_fp8_f32 v36, v12, v10
	v_med3_f32 v24, v24, s71, v223
	v_mul_f32_e32 v16, v16, v24
	v_mul_f32_e32 v16, v18, v16
	v_add_f32_e32 v35, 1.0, v41
	v_mov_b32_e32 v34, v181
	v_cvt_pk_fp8_f32 v36, v6, v16 op_sel:[0,0,1]
	v_fma_f32 v6, v174, s24, -v19
	v_rcp_f32_e32 v22, v22
	v_pk_mul_f32 v[34:35], v[34:35], s[26:27]
	v_mov_b32_e32 v37, v199
	v_max_f32_e32 v6, 0xc1898193, v6
	v_sub_f32_e32 v18, v34, v35
	v_cvt_pk_fp8_f32 v37, v14, v8
	v_exp_f32_e32 v12, v6
	v_med3_f32 v10, v18, s71, v223
	v_mul_f32_e32 v10, v20, v10
	v_mul_f32_e32 v10, v22, v10
	v_cvt_pk_fp8_f32 v37, v4, v10 op_sel:[0,0,1]
	v_add_f32_e32 v4, 1.0, v12
	v_rcp_f32_e32 v4, v4
	v_fma_f32 v8, v170, s24, -v17
	v_fma_f32 v12, v166, s26, -v23
	v_max_f32_e32 v8, 0xc1898193, v8
	v_med3_f32 v12, v12, s71, v223
	v_exp_f32_e32 v14, v8
	v_mul_f32_e32 v6, v6, v12
	v_mul_f32_e32 v4, v4, v6
	v_fma_f32 v6, v162, s26, -v21
	v_med3_f32 v6, v6, s71, v223
	v_mul_f32_e32 v6, v8, v6
	v_fma_f32 v8, v175, s24, -v11
	v_add_f32_e32 v10, 1.0, v14
	v_max_f32_e32 v8, 0xc1898193, v8
	v_rcp_f32_e32 v10, v10
	v_fma_f32 v12, v171, s24, -v9
	v_exp_f32_e32 v14, v8
	v_max_f32_e32 v12, 0xc1898193, v12
	v_exp_f32_e32 v16, v12
	v_mul_f32_e32 v6, v10, v6
	v_add_f32_e32 v10, 1.0, v14
	v_rcp_f32_e32 v10, v10
	v_add_f32_e32 v14, 1.0, v16
	v_fma_f32 v16, v167, s26, -v15
	v_med3_f32 v16, v16, s71, v223
	v_mul_f32_e32 v8, v8, v16
	v_mul_f32_e32 v8, v10, v8
	v_fma_f32 v10, v163, s26, -v13
	v_med3_f32 v10, v10, s71, v223
	v_mul_f32_e32 v10, v12, v10
	v_fma_f32 v12, v176, s24, -v7
	v_max_f32_e32 v12, 0xc1898193, v12
	v_rcp_f32_e32 v14, v14
	v_fma_f32 v16, v172, s24, -v5
	v_exp_f32_e32 v18, v12
	v_max_f32_e32 v16, 0xc1898193, v16
	v_exp_f32_e32 v20, v16
	v_mul_f32_e32 v10, v14, v10
	v_add_f32_e32 v14, 1.0, v18
	v_rcp_f32_e32 v14, v14
	v_add_f32_e32 v18, 1.0, v20
	v_fma_f32 v20, v168, s26, -v25
	v_med3_f32 v20, v20, s71, v223
	v_mul_f32_e32 v12, v12, v20
	v_mul_f32_e32 v12, v14, v12
	v_fma_f32 v14, v164, s26, -v27
	v_med3_f32 v14, v14, s71, v223
	v_mul_f32_e32 v14, v16, v14
	v_fma_f32 v16, v177, s24, -v29
	v_max_f32_e32 v16, 0xc1898193, v16
	v_rcp_f32_e32 v18, v18
	v_fma_f32 v20, v173, s24, -v31
	v_exp_f32_e32 v22, v16
	v_max_f32_e32 v20, 0xc1898193, v20
	v_exp_f32_e32 v24, v20
	v_mul_f32_e32 v14, v18, v14
	v_add_f32_e32 v18, 1.0, v22
	v_rcp_f32_e32 v18, v18
	v_add_f32_e32 v22, 1.0, v24
	v_fma_f32 v24, v169, s26, -v33
	v_med3_f32 v24, v24, s71, v223
	v_rcp_f32_e32 v22, v22
	v_mul_f32_e32 v16, v16, v24
	v_mov_b32_e32 v39, v199
	v_mul_f32_e32 v16, v18, v16
	v_fma_f32 v18, v165, s26, -v35
	v_cvt_pk_fp8_f32 v39, v6, v10
	v_med3_f32 v18, v18, s71, v223
	v_mov_b32_e32 v38, v199
	v_cvt_pk_fp8_f32 v38, v4, v8
	v_mul_f32_e32 v4, v20, v18
	v_mul_f32_e32 v4, v22, v4
	v_cvt_pk_fp8_f32 v39, v14, v4 op_sel:[0,0,1]
	v_fma_f32 v4, v158, s24, -v19
	v_max_f32_e32 v4, 0xc1898193, v4
	v_exp_f32_e32 v8, v4
	v_cvt_pk_fp8_f32 v38, v12, v16 op_sel:[0,0,1]
	v_fma_f32 v6, v154, s24, -v17
	v_fma_f32 v12, v150, s26, -v23
	v_add_f32_e32 v8, 1.0, v8
	v_rcp_f32_e32 v8, v8
	v_max_f32_e32 v6, 0xc1898193, v6
	v_med3_f32 v12, v12, s71, v223
	v_exp_f32_e32 v10, v6
	v_mul_f32_e32 v4, v4, v12
	v_mul_f32_e32 v4, v8, v4
	v_fma_f32 v8, v146, s26, -v21
	v_med3_f32 v8, v8, s71, v223
	v_mul_f32_e32 v6, v6, v8
	v_fma_f32 v8, v159, s24, -v11
	v_add_f32_e32 v10, 1.0, v10
	v_max_f32_e32 v8, 0xc1898193, v8
	v_rcp_f32_e32 v10, v10
	v_fma_f32 v12, v155, s24, -v9
	v_exp_f32_e32 v14, v8
	v_max_f32_e32 v12, 0xc1898193, v12
	v_exp_f32_e32 v16, v12
	v_mul_f32_e32 v6, v10, v6
	v_add_f32_e32 v10, 1.0, v14
	v_rcp_f32_e32 v10, v10
	v_add_f32_e32 v14, 1.0, v16
	v_fma_f32 v16, v151, s26, -v15
	v_med3_f32 v16, v16, s71, v223
	v_mul_f32_e32 v8, v8, v16
	v_mul_f32_e32 v8, v10, v8
	v_fma_f32 v10, v147, s26, -v13
	v_med3_f32 v10, v10, s71, v223
	v_mul_f32_e32 v10, v12, v10
	v_fma_f32 v12, v160, s24, -v7
	v_max_f32_e32 v12, 0xc1898193, v12
	v_rcp_f32_e32 v14, v14
	v_fma_f32 v16, v156, s24, -v5
	v_exp_f32_e32 v18, v12
	v_max_f32_e32 v16, 0xc1898193, v16
	v_exp_f32_e32 v20, v16
	v_mul_f32_e32 v10, v14, v10
	v_add_f32_e32 v14, 1.0, v18
	v_rcp_f32_e32 v14, v14
	v_add_f32_e32 v18, 1.0, v20
	v_fma_f32 v20, v152, s26, -v25
	v_med3_f32 v20, v20, s71, v223
	v_mul_f32_e32 v12, v12, v20
	v_mul_f32_e32 v12, v14, v12
	v_fma_f32 v14, v148, s26, -v27
	v_med3_f32 v14, v14, s71, v223
	v_mul_f32_e32 v14, v16, v14
	v_fma_f32 v16, v161, s24, -v29
	v_max_f32_e32 v16, 0xc1898193, v16
	v_rcp_f32_e32 v18, v18
	v_fma_f32 v20, v157, s24, -v31
	v_exp_f32_e32 v22, v16
	v_max_f32_e32 v20, 0xc1898193, v20
	v_exp_f32_e32 v24, v20
	v_mul_f32_e32 v14, v18, v14
	v_add_f32_e32 v18, 1.0, v22
	v_permlane16_swap_b32_e32 v36, v38
	v_permlane16_swap_b32_e32 v37, v39
	v_rcp_f32_e32 v18, v18
	global_store_dwordx4 v[2:3], v[36:39], off
	v_add_f32_e32 v22, 1.0, v24
	v_fma_f32 v24, v153, s26, -v33
	v_mov_b32_e32 v36, v199
	v_mov_b32_e32 v37, v199
	v_med3_f32 v24, v24, s71, v223
	v_cvt_pk_fp8_f32 v36, v4, v8
	v_cvt_pk_fp8_f32 v37, v6, v10
	v_fma_f32 v6, v142, s24, -v19
	v_rcp_f32_e32 v22, v22
	v_mul_f32_e32 v16, v16, v24
	v_max_f32_e32 v6, 0xc1898193, v6
	v_mul_f32_e32 v16, v18, v16
	v_fma_f32 v18, v149, s26, -v35
	v_fma_f32 v8, v138, s24, -v17
	v_exp_f32_e32 v10, v6
	v_med3_f32 v4, v18, s71, v223
	v_max_f32_e32 v8, 0xc1898193, v8
	v_mul_f32_e32 v4, v20, v4
	v_cvt_pk_fp8_f32 v36, v12, v16 op_sel:[0,0,1]
	v_exp_f32_e32 v12, v8
	v_mul_f32_e32 v4, v22, v4
	v_cvt_pk_fp8_f32 v37, v14, v4 op_sel:[0,0,1]
	v_add_f32_e32 v4, 1.0, v10
	v_rcp_f32_e32 v4, v4
	v_add_f32_e32 v10, 1.0, v12
	v_fma_f32 v12, v134, s26, -v23
	v_med3_f32 v12, v12, s71, v223
	v_mul_f32_e32 v6, v6, v12
	v_mul_f32_e32 v4, v4, v6
	v_fma_f32 v6, v130, s26, -v21
	v_med3_f32 v6, v6, s71, v223
	v_mul_f32_e32 v6, v8, v6
	v_fma_f32 v8, v143, s24, -v11
	v_max_f32_e32 v8, 0xc1898193, v8
	v_rcp_f32_e32 v10, v10
	v_fma_f32 v12, v139, s24, -v9
	v_exp_f32_e32 v14, v8
	v_max_f32_e32 v12, 0xc1898193, v12
	v_exp_f32_e32 v16, v12
	v_mul_f32_e32 v6, v10, v6
	v_add_f32_e32 v10, 1.0, v14
	v_rcp_f32_e32 v10, v10
	v_add_f32_e32 v14, 1.0, v16
	v_fma_f32 v16, v135, s26, -v15
	v_med3_f32 v16, v16, s71, v223
	v_mul_f32_e32 v8, v8, v16
	v_mul_f32_e32 v8, v10, v8
	v_fma_f32 v10, v131, s26, -v13
	v_med3_f32 v10, v10, s71, v223
	v_mul_f32_e32 v10, v12, v10
	v_fma_f32 v12, v144, s24, -v7
	v_max_f32_e32 v12, 0xc1898193, v12
	v_rcp_f32_e32 v14, v14
	v_fma_f32 v16, v140, s24, -v5
	v_exp_f32_e32 v18, v12
	v_max_f32_e32 v16, 0xc1898193, v16
	v_exp_f32_e32 v20, v16
	v_mul_f32_e32 v10, v14, v10
	v_add_f32_e32 v14, 1.0, v18
	v_rcp_f32_e32 v14, v14
	v_add_f32_e32 v18, 1.0, v20
	v_fma_f32 v20, v136, s26, -v25
	v_med3_f32 v20, v20, s71, v223
	v_mul_f32_e32 v12, v12, v20
	v_mul_f32_e32 v12, v14, v12
	v_fma_f32 v14, v132, s26, -v27
	v_med3_f32 v14, v14, s71, v223
	v_mul_f32_e32 v14, v16, v14
	v_fma_f32 v16, v145, s24, -v29
	v_max_f32_e32 v16, 0xc1898193, v16
	v_rcp_f32_e32 v18, v18
	v_fma_f32 v20, v141, s24, -v31
	v_exp_f32_e32 v22, v16
	v_max_f32_e32 v20, 0xc1898193, v20
	v_exp_f32_e32 v24, v20
	v_mul_f32_e32 v14, v18, v14
	v_add_f32_e32 v18, 1.0, v22
	v_rcp_f32_e32 v18, v18
	v_add_f32_e32 v22, 1.0, v24
	v_fma_f32 v24, v137, s26, -v33
	v_med3_f32 v24, v24, s71, v223
	v_rcp_f32_e32 v22, v22
	v_mul_f32_e32 v16, v16, v24
	v_mov_b32_e32 v39, v199
	v_mul_f32_e32 v16, v18, v16
	v_fma_f32 v18, v133, s26, -v35
	v_cvt_pk_fp8_f32 v39, v6, v10
	v_med3_f32 v18, v18, s71, v223
	v_mov_b32_e32 v38, v199
	v_cvt_pk_fp8_f32 v38, v4, v8
	v_mul_f32_e32 v4, v20, v18
	v_mul_f32_e32 v4, v22, v4
	v_cvt_pk_fp8_f32 v39, v14, v4 op_sel:[0,0,1]
	v_fma_f32 v4, v126, s24, -v19
	v_max_f32_e32 v4, 0xc1898193, v4
	v_exp_f32_e32 v8, v4
	v_cvt_pk_fp8_f32 v38, v12, v16 op_sel:[0,0,1]
	v_fma_f32 v6, v122, s24, -v17
	v_fma_f32 v12, v118, s26, -v23
	v_add_f32_e32 v8, 1.0, v8
	v_rcp_f32_e32 v8, v8
	v_max_f32_e32 v6, 0xc1898193, v6
	v_med3_f32 v12, v12, s71, v223
	v_exp_f32_e32 v10, v6
	v_mul_f32_e32 v4, v4, v12
	v_mul_f32_e32 v4, v8, v4
	v_fma_f32 v8, v114, s26, -v21
	v_med3_f32 v8, v8, s71, v223
	v_mul_f32_e32 v6, v6, v8
	v_fma_f32 v8, v127, s24, -v11
	v_add_f32_e32 v10, 1.0, v10
	v_max_f32_e32 v8, 0xc1898193, v8
	v_rcp_f32_e32 v10, v10
	v_fma_f32 v12, v123, s24, -v9
	v_exp_f32_e32 v14, v8
	v_max_f32_e32 v12, 0xc1898193, v12
	v_exp_f32_e32 v16, v12
	v_mul_f32_e32 v6, v10, v6
	v_add_f32_e32 v10, 1.0, v14
	v_rcp_f32_e32 v10, v10
	v_add_f32_e32 v14, 1.0, v16
	v_fma_f32 v16, v119, s26, -v15
	v_med3_f32 v16, v16, s71, v223
	v_mul_f32_e32 v8, v8, v16
	v_mul_f32_e32 v8, v10, v8
	v_fma_f32 v10, v115, s26, -v13
	v_med3_f32 v10, v10, s71, v223
	v_mul_f32_e32 v10, v12, v10
	v_fma_f32 v12, v128, s24, -v7
	v_max_f32_e32 v12, 0xc1898193, v12
	v_rcp_f32_e32 v14, v14
	v_fma_f32 v16, v124, s24, -v5
	v_exp_f32_e32 v18, v12
	v_max_f32_e32 v16, 0xc1898193, v16
	v_exp_f32_e32 v20, v16
	v_mul_f32_e32 v10, v14, v10
	v_add_f32_e32 v14, 1.0, v18
	v_rcp_f32_e32 v14, v14
	v_add_f32_e32 v18, 1.0, v20
	v_fma_f32 v20, v120, s26, -v25
	v_med3_f32 v20, v20, s71, v223
	v_mul_f32_e32 v12, v12, v20
	v_mul_f32_e32 v12, v14, v12
	v_fma_f32 v14, v116, s26, -v27
	v_med3_f32 v14, v14, s71, v223
	v_mul_f32_e32 v14, v16, v14
	v_fma_f32 v16, v129, s24, -v29
	v_max_f32_e32 v16, 0xc1898193, v16
	v_rcp_f32_e32 v18, v18
	v_fma_f32 v20, v125, s24, -v31
	v_exp_f32_e32 v22, v16
	v_max_f32_e32 v20, 0xc1898193, v20
	v_exp_f32_e32 v24, v20
	v_add_co_u32_e32 v40, vcc, s2, v2
	v_mul_f32_e32 v14, v18, v14
	v_add_f32_e32 v18, 1.0, v22
	v_permlane16_swap_b32_e32 v36, v38
	v_permlane16_swap_b32_e32 v37, v39
	v_addc_co_u32_e32 v41, vcc, 0, v3, vcc
	v_rcp_f32_e32 v18, v18
	global_store_dwordx4 v[40:41], v[36:39], off
	v_add_f32_e32 v22, 1.0, v24
	v_fma_f32 v24, v121, s26, -v33
	v_mov_b32_e32 v36, v199
	v_mov_b32_e32 v37, v199
	v_med3_f32 v24, v24, s71, v223
	v_cvt_pk_fp8_f32 v36, v4, v8
	v_cvt_pk_fp8_f32 v37, v6, v10
	v_fma_f32 v6, v110, s24, -v19
	v_rcp_f32_e32 v22, v22
	v_mul_f32_e32 v16, v16, v24
	v_max_f32_e32 v6, 0xc1898193, v6
	v_mul_f32_e32 v16, v18, v16
	v_fma_f32 v18, v117, s26, -v35
	v_fma_f32 v8, v106, s24, -v17
	v_exp_f32_e32 v10, v6
	v_med3_f32 v4, v18, s71, v223
	v_max_f32_e32 v8, 0xc1898193, v8
	v_mul_f32_e32 v4, v20, v4
	v_cvt_pk_fp8_f32 v36, v12, v16 op_sel:[0,0,1]
	v_exp_f32_e32 v12, v8
	v_mul_f32_e32 v4, v22, v4
	v_cvt_pk_fp8_f32 v37, v14, v4 op_sel:[0,0,1]
	v_add_f32_e32 v4, 1.0, v10
	v_rcp_f32_e32 v4, v4
	v_add_f32_e32 v10, 1.0, v12
	v_fma_f32 v12, v102, s26, -v23
	v_med3_f32 v12, v12, s71, v223
	v_mul_f32_e32 v6, v6, v12
	v_mul_f32_e32 v4, v4, v6
	v_fma_f32 v6, v90, s26, -v21
	v_med3_f32 v6, v6, s71, v223
	v_mul_f32_e32 v6, v8, v6
	v_fma_f32 v8, v111, s24, -v11
	v_max_f32_e32 v8, 0xc1898193, v8
	v_rcp_f32_e32 v10, v10
	v_fma_f32 v12, v107, s24, -v9
	v_exp_f32_e32 v14, v8
	v_max_f32_e32 v12, 0xc1898193, v12
	v_exp_f32_e32 v16, v12
	v_mul_f32_e32 v6, v10, v6
	v_add_f32_e32 v10, 1.0, v14
	v_rcp_f32_e32 v10, v10
	v_add_f32_e32 v14, 1.0, v16
	v_fma_f32 v16, v103, s26, -v15
	v_med3_f32 v16, v16, s71, v223
	v_mul_f32_e32 v8, v8, v16
	v_mul_f32_e32 v8, v10, v8
	v_fma_f32 v10, v91, s26, -v13
	v_med3_f32 v10, v10, s71, v223
	v_mul_f32_e32 v10, v12, v10
	v_fma_f32 v12, v112, s24, -v7
	v_max_f32_e32 v12, 0xc1898193, v12
	v_rcp_f32_e32 v14, v14
	v_fma_f32 v16, v108, s24, -v5
	v_exp_f32_e32 v18, v12
	v_max_f32_e32 v16, 0xc1898193, v16
	v_exp_f32_e32 v20, v16
	v_mul_f32_e32 v10, v14, v10
	v_add_f32_e32 v14, 1.0, v18
	v_rcp_f32_e32 v14, v14
	v_add_f32_e32 v18, 1.0, v20
	v_fma_f32 v20, v104, s26, -v25
	v_med3_f32 v20, v20, s71, v223
	v_mul_f32_e32 v12, v12, v20
	v_mul_f32_e32 v12, v14, v12
	v_fma_f32 v14, v92, s26, -v27
	v_med3_f32 v14, v14, s71, v223
	v_mul_f32_e32 v14, v16, v14
	v_fma_f32 v16, v113, s24, -v29
	v_max_f32_e32 v16, 0xc1898193, v16
	v_rcp_f32_e32 v18, v18
	v_fma_f32 v20, v109, s24, -v31
	v_exp_f32_e32 v22, v16
	v_max_f32_e32 v20, 0xc1898193, v20
	v_exp_f32_e32 v24, v20
	v_mul_f32_e32 v14, v18, v14
	v_add_f32_e32 v18, 1.0, v22
	v_rcp_f32_e32 v18, v18
	v_add_f32_e32 v22, 1.0, v24
	v_fma_f32 v24, v105, s26, -v33
	v_med3_f32 v24, v24, s71, v223
	v_rcp_f32_e32 v22, v22
	v_mul_f32_e32 v16, v16, v24
	v_mov_b32_e32 v39, v199
	v_mul_f32_e32 v16, v18, v16
	v_fma_f32 v18, v93, s26, -v35
	v_cvt_pk_fp8_f32 v39, v6, v10
	v_med3_f32 v18, v18, s71, v223
	v_mov_b32_e32 v38, v199
	v_cvt_pk_fp8_f32 v38, v4, v8
	v_mul_f32_e32 v4, v20, v18
	v_mul_f32_e32 v4, v22, v4
	v_cvt_pk_fp8_f32 v39, v14, v4 op_sel:[0,0,1]
	v_fma_f32 v4, v86, s24, -v19
	v_max_f32_e32 v4, 0xc1898193, v4
	v_exp_f32_e32 v8, v4
	v_cvt_pk_fp8_f32 v38, v12, v16 op_sel:[0,0,1]
	v_fma_f32 v6, v82, s24, -v17
	v_fma_f32 v12, v94, s26, -v23
	v_add_f32_e32 v8, 1.0, v8
	v_rcp_f32_e32 v8, v8
	v_max_f32_e32 v6, 0xc1898193, v6
	v_med3_f32 v12, v12, s71, v223
	v_exp_f32_e32 v10, v6
	v_mul_f32_e32 v4, v4, v12
	v_mul_f32_e32 v4, v8, v4
	v_fma_f32 v8, v98, s26, -v21
	v_med3_f32 v8, v8, s71, v223
	v_mul_f32_e32 v6, v6, v8
	v_fma_f32 v8, v87, s24, -v11
	v_add_f32_e32 v10, 1.0, v10
	v_max_f32_e32 v8, 0xc1898193, v8
	v_rcp_f32_e32 v10, v10
	v_fma_f32 v12, v83, s24, -v9
	v_exp_f32_e32 v14, v8
	v_max_f32_e32 v12, 0xc1898193, v12
	v_exp_f32_e32 v16, v12
	v_mul_f32_e32 v6, v10, v6
	v_add_f32_e32 v10, 1.0, v14
	v_rcp_f32_e32 v10, v10
	v_add_f32_e32 v14, 1.0, v16
	v_fma_f32 v16, v95, s26, -v15
	v_med3_f32 v16, v16, s71, v223
	v_mul_f32_e32 v8, v8, v16
	v_mul_f32_e32 v8, v10, v8
	v_fma_f32 v10, v99, s26, -v13
	v_med3_f32 v10, v10, s71, v223
	v_mul_f32_e32 v10, v12, v10
	v_fma_f32 v12, v88, s24, -v7
	v_max_f32_e32 v12, 0xc1898193, v12
	v_rcp_f32_e32 v14, v14
	v_fma_f32 v16, v84, s24, -v5
	v_exp_f32_e32 v18, v12
	v_max_f32_e32 v16, 0xc1898193, v16
	v_exp_f32_e32 v20, v16
	v_mul_f32_e32 v10, v14, v10
	v_add_f32_e32 v14, 1.0, v18
	v_rcp_f32_e32 v14, v14
	v_add_f32_e32 v18, 1.0, v20
	v_fma_f32 v20, v96, s26, -v25
	v_med3_f32 v20, v20, s71, v223
	v_mul_f32_e32 v12, v12, v20
	v_mul_f32_e32 v12, v14, v12
	v_fma_f32 v14, v100, s26, -v27
	v_med3_f32 v14, v14, s71, v223
	v_mul_f32_e32 v14, v16, v14
	v_fma_f32 v16, v89, s24, -v29
	v_max_f32_e32 v16, 0xc1898193, v16
	v_rcp_f32_e32 v18, v18
	v_fma_f32 v20, v85, s24, -v31
	v_exp_f32_e32 v22, v16
	v_max_f32_e32 v20, 0xc1898193, v20
	v_exp_f32_e32 v24, v20
	s_mov_b32 s2, 0x20000
	v_add_co_u32_e32 v40, vcc, s2, v2
	v_mul_f32_e32 v14, v18, v14
	v_add_f32_e32 v18, 1.0, v22
	v_permlane16_swap_b32_e32 v36, v38
	v_permlane16_swap_b32_e32 v37, v39
	v_addc_co_u32_e32 v41, vcc, 0, v3, vcc
	v_rcp_f32_e32 v18, v18
	global_store_dwordx4 v[40:41], v[36:39], off
	v_add_f32_e32 v22, 1.0, v24
	v_fma_f32 v24, v97, s26, -v33
	v_mov_b32_e32 v36, v199
	v_mov_b32_e32 v37, v199
	v_med3_f32 v24, v24, s71, v223
	v_cvt_pk_fp8_f32 v36, v4, v8
	v_cvt_pk_fp8_f32 v37, v6, v10
	v_fma_f32 v6, v70, s24, -v19
	v_rcp_f32_e32 v22, v22
	v_mul_f32_e32 v16, v16, v24
	v_max_f32_e32 v6, 0xc1898193, v6
	v_mul_f32_e32 v16, v18, v16
	v_fma_f32 v18, v101, s26, -v35
	v_fma_f32 v8, v66, s24, -v17
	v_exp_f32_e32 v10, v6
	v_med3_f32 v4, v18, s71, v223
	v_max_f32_e32 v8, 0xc1898193, v8
	v_mul_f32_e32 v4, v20, v4
	v_cvt_pk_fp8_f32 v36, v12, v16 op_sel:[0,0,1]
	v_exp_f32_e32 v12, v8
	v_mul_f32_e32 v4, v22, v4
	v_cvt_pk_fp8_f32 v37, v14, v4 op_sel:[0,0,1]
	v_add_f32_e32 v4, 1.0, v10
	v_rcp_f32_e32 v4, v4
	v_add_f32_e32 v10, 1.0, v12
	v_fma_f32 v12, v74, s26, -v23
	v_med3_f32 v12, v12, s71, v223
	v_mul_f32_e32 v6, v6, v12
	v_mul_f32_e32 v4, v4, v6
	v_fma_f32 v6, v78, s26, -v21
	v_med3_f32 v6, v6, s71, v223
	v_mul_f32_e32 v6, v8, v6
	v_fma_f32 v8, v71, s24, -v11
	v_max_f32_e32 v8, 0xc1898193, v8
	v_rcp_f32_e32 v10, v10
	v_fma_f32 v9, v67, s24, -v9
	v_exp_f32_e32 v11, v8
	v_max_f32_e32 v9, 0xc1898193, v9
	v_exp_f32_e32 v12, v9
	v_mul_f32_e32 v6, v10, v6
	v_add_f32_e32 v10, 1.0, v11
	v_rcp_f32_e32 v10, v10
	v_add_f32_e32 v11, 1.0, v12
	v_fma_f32 v12, v75, s26, -v15
	v_med3_f32 v12, v12, s71, v223
	v_mul_f32_e32 v8, v8, v12
	v_mul_f32_e32 v8, v10, v8
	v_fma_f32 v10, v79, s26, -v13
	v_fma_f32 v7, v72, s24, -v7
	v_med3_f32 v10, v10, s71, v223
	v_max_f32_e32 v7, 0xc1898193, v7
	v_mul_f32_e32 v9, v9, v10
	v_fma_f32 v5, v68, s24, -v5
	v_exp_f32_e32 v10, v7
	v_max_f32_e32 v5, 0xc1898193, v5
	v_rcp_f32_e32 v11, v11
	v_exp_f32_e32 v12, v5
	v_add_f32_e32 v10, 1.0, v10
	v_rcp_f32_e32 v10, v10
	v_mul_f32_e32 v9, v11, v9
	v_add_f32_e32 v11, 1.0, v12
	v_fma_f32 v12, v76, s26, -v25
	v_med3_f32 v12, v12, s71, v223
	v_mul_f32_e32 v7, v7, v12
	v_mul_f32_e32 v7, v10, v7
	v_fma_f32 v10, v80, s26, -v27
	v_med3_f32 v10, v10, s71, v223
	v_mul_f32_e32 v5, v5, v10
	v_fma_f32 v10, v73, s24, -v29
	v_max_f32_e32 v10, 0xc1898193, v10
	v_rcp_f32_e32 v11, v11
	v_fma_f32 v12, v69, s24, -v31
	v_exp_f32_e32 v13, v10
	v_max_f32_e32 v12, 0xc1898193, v12
	v_exp_f32_e32 v14, v12
	v_mul_f32_e32 v5, v11, v5
	v_add_f32_e32 v11, 1.0, v13
	v_rcp_f32_e32 v11, v11
	v_add_f32_e32 v13, 1.0, v14
	v_fma_f32 v14, v77, s26, -v33
	v_med3_f32 v14, v14, s71, v223
	v_rcp_f32_e32 v13, v13
	v_mul_f32_e32 v10, v10, v14
	v_mov_b32_e32 v38, v199
	v_mov_b32_e32 v39, v199
	v_mul_f32_e32 v10, v11, v10
	v_fma_f32 v11, v81, s26, -v35
	v_cvt_pk_fp8_f32 v38, v4, v8
	v_cvt_pk_fp8_f32 v39, v6, v9
	v_med3_f32 v11, v11, s71, v223
	v_mul_f32_e32 v4, v12, v11
	v_mul_f32_e32 v4, v13, v4
	v_cvt_pk_fp8_f32 v38, v7, v10 op_sel:[0,0,1]
	v_cvt_pk_fp8_f32 v39, v5, v4 op_sel:[0,0,1]
	v_add_co_u32_e32 v2, vcc, 0x28000, v2
	v_permlane16_swap_b32_e32 v36, v38
	s_nop 0
	v_addc_co_u32_e32 v3, vcc, 0, v3, vcc
	v_permlane16_swap_b32_e32 v37, v39
	s_and_b64 vcc, exec, s[4:5]
	s_mov_b64 s[4:5], -1
	global_store_dwordx4 v[2:3], v[36:39], off
	s_cbranch_vccnz .LBB0_975
	s_andn2_b64 vcc, exec, s[16:17]
	s_cbranch_vccnz .LBB0_974
	s_barrier
	s_branch .LBB0_974

.LBB0_1090:
	v_lshl_add_u32 v2, s27, 8, v215
	v_ashrrev_i32_e32 v3, 31, v2
	s_ashr_i32 s0, s84, 2
	s_lshl_b32 s1, s84, 8
	v_lshl_add_u64 v[4:5], v[2:3], 2, s[92:93]
	v_add_u32_e32 v6, 0x80, v2
	v_add_u32_e32 v8, 0x90, v2
	v_add_u32_e32 v10, 0xa0, v2
	v_add_u32_e32 v2, 0xb0, v2
	s_and_b32 s84, s1, 0x300
	v_ashrrev_i32_e32 v3, 31, v2
	s_ashr_i32 s1, s0, 31
	s_waitcnt vmcnt(0)
	v_ashrrev_i32_e32 v7, 31, v6
	v_ashrrev_i32_e32 v9, 31, v8
	v_ashrrev_i32_e32 v11, 31, v10
	v_lshl_add_u64 v[2:3], v[2:3], 2, s[92:93]
	s_lshl_b64 s[0:1], s[0:1], 12
	v_readlane_b32 s50, v239, 17
	v_lshl_add_u64 v[6:7], v[6:7], 2, s[92:93]
	v_lshl_add_u64 v[8:9], v[8:9], 2, s[92:93]
	v_lshl_add_u64 v[10:11], v[10:11], 2, s[92:93]
	global_load_dword v34, v[4:5], off
	global_load_dword v36, v[4:5], off offset:64
	global_load_dword v38, v[4:5], off offset:128
	global_load_dword v26, v[4:5], off offset:192
	global_load_dword v24, v[6:7], off
	global_load_dword v22, v[8:9], off
	global_load_dword v20, v[10:11], off
	global_load_dword v18, v[2:3], off
	v_or_b32_e32 v2, s84, v217
	v_readlane_b32 s51, v239, 18
	s_add_u32 s0, s50, s0
	s_addc_u32 s1, s51, s1
	v_lshlrev_b32_e32 v2, 2, v2
	global_load_dwordx4 v[14:17], v2, s[0:1]
	global_load_dwordx4 v[10:13], v2, s[0:1] offset:16
	global_load_dwordx4 v[6:9], v2, s[0:1] offset:128
	s_nop 0
	global_load_dwordx4 v[2:5], v2, s[0:1] offset:144
	v_mov_b32_e32 v28, v199
	v_mov_b32_e32 v29, v199
	v_mov_b32_e32 v30, v199
	v_mov_b32_e32 v31, v199
	v_mov_b32_e32 v32, v199
	v_mov_b32_e32 v33, v199
	s_waitcnt vmcnt(0)
	v_ashrrev_i32_e32 v35, 31, v34
	v_lshlrev_b64 v[40:41], 10, v[34:35]
	v_cmp_lt_i64_e32 vcc, -1, v[34:35]
	v_ashrrev_i32_e32 v37, 31, v36
	v_lshlrev_b64 v[42:43], 10, v[36:37]
	v_cndmask_b32_e32 v35, 0, v41, vcc
	v_cndmask_b32_e32 v34, v221, v40, vcc
	v_cmp_lt_i64_e64 s[0:1], -1, v[36:37]
	v_lshl_add_u64 v[34:35], s[94:95], 0, v[34:35]
	v_lshl_add_u64 v[34:35], v[34:35], 0, s[84:85]
	v_pk_fma_f32 v[40:41], v[190:191], s[8:9], v[14:15] op_sel_hi:[1,0,1]
	v_pk_fma_f32 v[46:47], v[186:187], s[8:9], v[10:11] op_sel_hi:[1,0,1]
	v_pk_fma_f32 v[50:51], v[174:175], s[8:9], v[6:7] op_sel_hi:[1,0,1]
	v_pk_fma_f32 v[54:55], v[170:171], s[8:9], v[2:3] op_sel_hi:[1,0,1]
	v_cvt_pk_fp8_f32 v28, v40, v41
	v_cvt_pk_fp8_f32 v29, v46, v47
	v_cvt_pk_fp8_f32 v30, v50, v51
	v_cvt_pk_fp8_f32 v31, v54, v55
	v_pk_fma_f32 v[36:37], v[192:193], s[8:9], v[16:17] op_sel_hi:[1,0,1]
	v_pk_fma_f32 v[44:45], v[188:189], s[8:9], v[12:13] op_sel_hi:[1,0,1]
	v_pk_fma_f32 v[48:49], v[176:177], s[8:9], v[8:9] op_sel_hi:[1,0,1]
	v_pk_fma_f32 v[52:53], v[172:173], s[8:9], v[4:5] op_sel_hi:[1,0,1]
	v_cvt_pk_fp8_f32 v28, v36, v37 op_sel:[0,0,1]
	v_cvt_pk_fp8_f32 v29, v44, v45 op_sel:[0,0,1]
	v_cvt_pk_fp8_f32 v30, v48, v49 op_sel:[0,0,1]
	v_cvt_pk_fp8_f32 v31, v52, v53 op_sel:[0,0,1]
	v_lshl_add_u64 v[34:35], v[34:35], 0, s[6:7]
	v_lshl_add_u64 v[34:35], v[34:35], 0, v[202:203]
	v_permlane16_swap_b32_e32 v28, v30
	v_permlane16_swap_b32_e32 v29, v31
	v_pk_fma_f32 v[58:59], v[182:183], s[8:9], v[14:15] op_sel_hi:[1,0,1]
	v_pk_fma_f32 v[62:63], v[178:179], s[8:9], v[10:11] op_sel_hi:[1,0,1]
	global_store_dwordx4 v[34:35], v[28:31], off
	v_mov_b32_e32 v34, v199
	v_mov_b32_e32 v35, v199
	v_pk_fma_f32 v[28:29], v[166:167], s[8:9], v[6:7] op_sel_hi:[1,0,1]
	v_pk_fma_f32 v[30:31], v[162:163], s[8:9], v[2:3] op_sel_hi:[1,0,1]
	v_cvt_pk_fp8_f32 v32, v58, v59
	v_cvt_pk_fp8_f32 v33, v62, v63
	v_cvt_pk_fp8_f32 v34, v28, v29
	v_cvt_pk_fp8_f32 v35, v30, v31
	v_pk_fma_f32 v[56:57], v[184:185], s[8:9], v[16:17] op_sel_hi:[1,0,1]
	v_pk_fma_f32 v[60:61], v[180:181], s[8:9], v[12:13] op_sel_hi:[1,0,1]
	v_pk_fma_f32 v[28:29], v[168:169], s[8:9], v[8:9] op_sel_hi:[1,0,1]
	v_pk_fma_f32 v[30:31], v[164:165], s[8:9], v[4:5] op_sel_hi:[1,0,1]
	v_cndmask_b32_e64 v43, 0, v43, s[0:1]
	v_cndmask_b32_e64 v42, v221, v42, s[0:1]
	v_cvt_pk_fp8_f32 v32, v56, v57 op_sel:[0,0,1]
	v_cvt_pk_fp8_f32 v33, v60, v61 op_sel:[0,0,1]
	v_cvt_pk_fp8_f32 v34, v28, v29 op_sel:[0,0,1]
	v_cvt_pk_fp8_f32 v35, v30, v31 op_sel:[0,0,1]
	v_lshl_add_u64 v[40:41], s[94:95], 0, v[42:43]
	v_lshl_add_u64 v[40:41], v[40:41], 0, s[84:85]
	v_lshl_add_u64 v[40:41], v[40:41], 0, s[6:7]
	v_ashrrev_i32_e32 v39, 31, v38
	v_lshl_add_u64 v[28:29], v[40:41], 0, v[202:203]
	v_permlane16_swap_b32_e32 v32, v34
	v_permlane16_swap_b32_e32 v33, v35
	global_store_dwordx4 v[28:29], v[32:35], off
	v_lshlrev_b64 v[28:29], 10, v[38:39]
	v_cmp_lt_i64_e32 vcc, -1, v[38:39]
	v_pk_fma_f32 v[30:31], v[158:159], s[8:9], v[14:15] op_sel_hi:[1,0,1]
	v_pk_fma_f32 v[34:35], v[154:155], s[8:9], v[10:11] op_sel_hi:[1,0,1]
	v_cndmask_b32_e32 v29, 0, v29, vcc
	v_cndmask_b32_e32 v28, v221, v28, vcc
	v_lshl_add_u64 v[28:29], s[94:95], 0, v[28:29]
	v_lshl_add_u64 v[28:29], v[28:29], 0, s[84:85]
	v_lshl_add_u64 v[32:33], v[28:29], 0, s[6:7]
	v_mov_b32_e32 v28, v199
	v_mov_b32_e32 v29, v199
	v_cvt_pk_fp8_f32 v28, v30, v31
	v_cvt_pk_fp8_f32 v29, v34, v35
	v_pk_fma_f32 v[30:31], v[160:161], s[8:9], v[16:17] op_sel_hi:[1,0,1]
	v_pk_fma_f32 v[34:35], v[156:157], s[8:9], v[12:13] op_sel_hi:[1,0,1]
	v_cvt_pk_fp8_f32 v28, v30, v31 op_sel:[0,0,1]
	v_cvt_pk_fp8_f32 v29, v34, v35 op_sel:[0,0,1]
	v_pk_fma_f32 v[34:35], v[150:151], s[8:9], v[6:7] op_sel_hi:[1,0,1]
	v_pk_fma_f32 v[36:37], v[146:147], s[8:9], v[2:3] op_sel_hi:[1,0,1]
	v_mov_b32_e32 v30, v199
	v_mov_b32_e32 v31, v199
	v_cvt_pk_fp8_f32 v30, v34, v35
	v_cvt_pk_fp8_f32 v31, v36, v37
	v_pk_fma_f32 v[34:35], v[152:153], s[8:9], v[8:9] op_sel_hi:[1,0,1]
	v_pk_fma_f32 v[36:37], v[148:149], s[8:9], v[4:5] op_sel_hi:[1,0,1]
	v_cvt_pk_fp8_f32 v30, v34, v35 op_sel:[0,0,1]
	v_cvt_pk_fp8_f32 v31, v36, v37 op_sel:[0,0,1]
	v_ashrrev_i32_e32 v27, 31, v26
	v_lshl_add_u64 v[32:33], v[32:33], 0, v[202:203]
	v_permlane16_swap_b32_e32 v28, v30
	v_permlane16_swap_b32_e32 v29, v31
	global_store_dwordx4 v[32:33], v[28:31], off
	v_cmp_lt_i64_e32 vcc, -1, v[26:27]
	v_pk_fma_f32 v[32:33], v[138:139], s[8:9], v[10:11] op_sel_hi:[1,0,1]
	v_lshlrev_b64 v[28:29], 10, v[26:27]
	v_cndmask_b32_e32 v27, 0, v29, vcc
	v_cndmask_b32_e32 v26, v221, v28, vcc
	v_lshl_add_u64 v[26:27], s[94:95], 0, v[26:27]
	v_lshl_add_u64 v[26:27], v[26:27], 0, s[84:85]
	v_lshl_add_u64 v[30:31], v[26:27], 0, s[6:7]
	v_pk_fma_f32 v[28:29], v[142:143], s[8:9], v[14:15] op_sel_hi:[1,0,1]
	v_mov_b32_e32 v26, v199
	v_mov_b32_e32 v27, v199
	v_cvt_pk_fp8_f32 v26, v28, v29
	v_cvt_pk_fp8_f32 v27, v32, v33
	v_pk_fma_f32 v[28:29], v[144:145], s[8:9], v[16:17] op_sel_hi:[1,0,1]
	v_pk_fma_f32 v[32:33], v[140:141], s[8:9], v[12:13] op_sel_hi:[1,0,1]
	v_cvt_pk_fp8_f32 v26, v28, v29 op_sel:[0,0,1]
	v_cvt_pk_fp8_f32 v27, v32, v33 op_sel:[0,0,1]
	v_pk_fma_f32 v[32:33], v[134:135], s[8:9], v[6:7] op_sel_hi:[1,0,1]
	v_pk_fma_f32 v[34:35], v[130:131], s[8:9], v[2:3] op_sel_hi:[1,0,1]
	v_mov_b32_e32 v28, v199
	v_mov_b32_e32 v29, v199
	v_cvt_pk_fp8_f32 v28, v32, v33
	v_cvt_pk_fp8_f32 v29, v34, v35
	v_pk_fma_f32 v[32:33], v[136:137], s[8:9], v[8:9] op_sel_hi:[1,0,1]
	v_pk_fma_f32 v[34:35], v[132:133], s[8:9], v[4:5] op_sel_hi:[1,0,1]
	v_cvt_pk_fp8_f32 v28, v32, v33 op_sel:[0,0,1]
	v_cvt_pk_fp8_f32 v29, v34, v35 op_sel:[0,0,1]
	v_ashrrev_i32_e32 v25, 31, v24
	v_lshl_add_u64 v[30:31], v[30:31], 0, v[202:203]
	v_permlane16_swap_b32_e32 v26, v28
	v_permlane16_swap_b32_e32 v27, v29
	global_store_dwordx4 v[30:31], v[26:29], off
	v_cmp_lt_i64_e32 vcc, -1, v[24:25]
	v_pk_fma_f32 v[30:31], v[122:123], s[8:9], v[10:11] op_sel_hi:[1,0,1]
	v_lshlrev_b64 v[26:27], 10, v[24:25]
	v_cndmask_b32_e32 v25, 0, v27, vcc
	v_cndmask_b32_e32 v24, v221, v26, vcc
	v_lshl_add_u64 v[24:25], s[94:95], 0, v[24:25]
	v_lshl_add_u64 v[24:25], v[24:25], 0, s[84:85]
	v_lshl_add_u64 v[28:29], v[24:25], 0, s[6:7]
	v_pk_fma_f32 v[26:27], v[126:127], s[8:9], v[14:15] op_sel_hi:[1,0,1]
	v_mov_b32_e32 v24, v199
	v_mov_b32_e32 v25, v199
	v_cvt_pk_fp8_f32 v24, v26, v27
	v_cvt_pk_fp8_f32 v25, v30, v31
	v_pk_fma_f32 v[26:27], v[128:129], s[8:9], v[16:17] op_sel_hi:[1,0,1]
	v_pk_fma_f32 v[30:31], v[124:125], s[8:9], v[12:13] op_sel_hi:[1,0,1]
	v_cvt_pk_fp8_f32 v24, v26, v27 op_sel:[0,0,1]
	v_cvt_pk_fp8_f32 v25, v30, v31 op_sel:[0,0,1]
	v_pk_fma_f32 v[30:31], v[118:119], s[8:9], v[6:7] op_sel_hi:[1,0,1]
	v_pk_fma_f32 v[32:33], v[114:115], s[8:9], v[2:3] op_sel_hi:[1,0,1]
	v_mov_b32_e32 v26, v199
	v_mov_b32_e32 v27, v199
	v_cvt_pk_fp8_f32 v26, v30, v31
	v_cvt_pk_fp8_f32 v27, v32, v33
	v_pk_fma_f32 v[30:31], v[120:121], s[8:9], v[8:9] op_sel_hi:[1,0,1]
	v_pk_fma_f32 v[32:33], v[116:117], s[8:9], v[4:5] op_sel_hi:[1,0,1]
	v_cvt_pk_fp8_f32 v26, v30, v31 op_sel:[0,0,1]
	v_cvt_pk_fp8_f32 v27, v32, v33 op_sel:[0,0,1]
	v_ashrrev_i32_e32 v23, 31, v22
	v_lshl_add_u64 v[28:29], v[28:29], 0, v[202:203]
	v_permlane16_swap_b32_e32 v24, v26
	v_permlane16_swap_b32_e32 v25, v27
	global_store_dwordx4 v[28:29], v[24:27], off
	v_cmp_lt_i64_e32 vcc, -1, v[22:23]
	v_pk_fma_f32 v[28:29], v[98:99], s[8:9], v[10:11] op_sel_hi:[1,0,1]
	v_lshlrev_b64 v[24:25], 10, v[22:23]
	v_cndmask_b32_e32 v23, 0, v25, vcc
	v_cndmask_b32_e32 v22, v221, v24, vcc
	v_lshl_add_u64 v[22:23], s[94:95], 0, v[22:23]
	v_lshl_add_u64 v[22:23], v[22:23], 0, s[84:85]
	v_lshl_add_u64 v[26:27], v[22:23], 0, s[6:7]
	v_pk_fma_f32 v[24:25], v[106:107], s[8:9], v[14:15] op_sel_hi:[1,0,1]
	v_mov_b32_e32 v22, v199
	v_mov_b32_e32 v23, v199
	v_cvt_pk_fp8_f32 v22, v24, v25
	v_cvt_pk_fp8_f32 v23, v28, v29
	v_pk_fma_f32 v[24:25], v[108:109], s[8:9], v[16:17] op_sel_hi:[1,0,1]
	v_pk_fma_f32 v[28:29], v[100:101], s[8:9], v[12:13] op_sel_hi:[1,0,1]
	v_cvt_pk_fp8_f32 v22, v24, v25 op_sel:[0,0,1]
	v_cvt_pk_fp8_f32 v23, v28, v29 op_sel:[0,0,1]
	v_pk_fma_f32 v[28:29], v[90:91], s[8:9], v[6:7] op_sel_hi:[1,0,1]
	v_pk_fma_f32 v[30:31], v[82:83], s[8:9], v[2:3] op_sel_hi:[1,0,1]
	v_mov_b32_e32 v24, v199
	v_mov_b32_e32 v25, v199
	v_cvt_pk_fp8_f32 v24, v28, v29
	v_cvt_pk_fp8_f32 v25, v30, v31
	v_pk_fma_f32 v[28:29], v[92:93], s[8:9], v[8:9] op_sel_hi:[1,0,1]
	v_pk_fma_f32 v[30:31], v[84:85], s[8:9], v[4:5] op_sel_hi:[1,0,1]
	v_cvt_pk_fp8_f32 v24, v28, v29 op_sel:[0,0,1]
	v_cvt_pk_fp8_f32 v25, v30, v31 op_sel:[0,0,1]
	v_ashrrev_i32_e32 v21, 31, v20
	v_lshl_add_u64 v[26:27], v[26:27], 0, v[202:203]
	v_permlane16_swap_b32_e32 v22, v24
	v_permlane16_swap_b32_e32 v23, v25
	global_store_dwordx4 v[26:27], v[22:25], off
	v_cmp_lt_i64_e32 vcc, -1, v[20:21]
	v_pk_fma_f32 v[26:27], v[74:75], s[8:9], v[10:11] op_sel_hi:[1,0,1]
	v_lshlrev_b64 v[22:23], 10, v[20:21]
	v_cndmask_b32_e32 v21, 0, v23, vcc
	v_cndmask_b32_e32 v20, v221, v22, vcc
	v_lshl_add_u64 v[20:21], s[94:95], 0, v[20:21]
	v_lshl_add_u64 v[20:21], v[20:21], 0, s[84:85]
	v_lshl_add_u64 v[24:25], v[20:21], 0, s[6:7]
	v_pk_fma_f32 v[22:23], v[78:79], s[8:9], v[14:15] op_sel_hi:[1,0,1]
	v_mov_b32_e32 v20, v199
	v_mov_b32_e32 v21, v199
	v_cvt_pk_fp8_f32 v20, v22, v23
	v_cvt_pk_fp8_f32 v21, v26, v27
	v_pk_fma_f32 v[22:23], v[80:81], s[8:9], v[16:17] op_sel_hi:[1,0,1]
	v_pk_fma_f32 v[26:27], v[76:77], s[8:9], v[12:13] op_sel_hi:[1,0,1]
	v_cvt_pk_fp8_f32 v20, v22, v23 op_sel:[0,0,1]
	v_cvt_pk_fp8_f32 v21, v26, v27 op_sel:[0,0,1]
	v_pk_fma_f32 v[26:27], v[102:103], s[8:9], v[6:7] op_sel_hi:[1,0,1]
	v_pk_fma_f32 v[28:29], v[110:111], s[8:9], v[2:3] op_sel_hi:[1,0,1]
	v_mov_b32_e32 v22, v199
	v_mov_b32_e32 v23, v199
	v_cvt_pk_fp8_f32 v22, v26, v27
	v_cvt_pk_fp8_f32 v23, v28, v29
	v_pk_fma_f32 v[26:27], v[104:105], s[8:9], v[8:9] op_sel_hi:[1,0,1]
	v_pk_fma_f32 v[28:29], v[112:113], s[8:9], v[4:5] op_sel_hi:[1,0,1]
	v_cvt_pk_fp8_f32 v22, v26, v27 op_sel:[0,0,1]
	v_cvt_pk_fp8_f32 v23, v28, v29 op_sel:[0,0,1]
	v_ashrrev_i32_e32 v19, 31, v18
	v_lshl_add_u64 v[24:25], v[24:25], 0, v[202:203]
	v_permlane16_swap_b32_e32 v20, v22
	v_permlane16_swap_b32_e32 v21, v23
	global_store_dwordx4 v[24:25], v[20:23], off
	v_cmp_lt_i64_e32 vcc, -1, v[18:19]
	v_pk_fma_f32 v[12:13], v[68:69], s[8:9], v[12:13] op_sel_hi:[1,0,1]
	v_lshlrev_b64 v[20:21], 10, v[18:19]
	v_cndmask_b32_e32 v19, 0, v21, vcc
	v_cndmask_b32_e32 v18, v221, v20, vcc
	v_pk_fma_f32 v[20:21], v[66:67], s[8:9], v[10:11] op_sel_hi:[1,0,1]
	v_mov_b32_e32 v11, v199
	v_cvt_pk_fp8_f32 v11, v20, v21
	v_pk_fma_f32 v[14:15], v[70:71], s[8:9], v[14:15] op_sel_hi:[1,0,1]
	v_mov_b32_e32 v10, v199
	v_pk_fma_f32 v[6:7], v[86:87], s[8:9], v[6:7] op_sel_hi:[1,0,1]
	v_cvt_pk_fp8_f32 v11, v12, v13 op_sel:[0,0,1]
	v_pk_fma_f32 v[2:3], v[94:95], s[8:9], v[2:3] op_sel_hi:[1,0,1]
	v_mov_b32_e32 v12, v199
	v_mov_b32_e32 v13, v199
	v_cvt_pk_fp8_f32 v10, v14, v15
	v_cvt_pk_fp8_f32 v12, v6, v7
	v_cvt_pk_fp8_f32 v13, v2, v3
	v_pk_fma_f32 v[14:15], v[72:73], s[8:9], v[16:17] op_sel_hi:[1,0,1]
	v_pk_fma_f32 v[2:3], v[88:89], s[8:9], v[8:9] op_sel_hi:[1,0,1]
	v_pk_fma_f32 v[4:5], v[96:97], s[8:9], v[4:5] op_sel_hi:[1,0,1]
	v_cvt_pk_fp8_f32 v10, v14, v15 op_sel:[0,0,1]
	v_cvt_pk_fp8_f32 v12, v2, v3 op_sel:[0,0,1]
	v_cvt_pk_fp8_f32 v13, v4, v5 op_sel:[0,0,1]
	v_lshl_add_u64 v[18:19], s[94:95], 0, v[18:19]
	v_lshl_add_u64 v[18:19], v[18:19], 0, s[84:85]
	v_lshl_add_u64 v[18:19], v[18:19], 0, s[6:7]
	v_lshl_add_u64 v[2:3], v[18:19], 0, v[202:203]
	v_permlane16_swap_b32_e32 v10, v12
	v_permlane16_swap_b32_e32 v11, v13
	s_and_b64 vcc, exec, s[2:3]
	s_mov_b64 s[0:1], -1
	global_store_dwordx4 v[2:3], v[10:13], off
	s_cbranch_vccnz .LBB0_1076
	s_andn2_b64 vcc, exec, s[90:91]
	s_cbranch_vccnz .LBB0_1075
	s_barrier
	s_branch .LBB0_1075
